# attnA reorder: QK MFMA then exp/cvt then PV then max chain; p0 exps moved to tile tail
# speedup vs baseline: 1.0057x; 1.0057x over previous
.LBB0_419:
	s_lshl_b32 s8, s57, 13
	s_add_i32 s8, s8, 0
	v_add_u32_e32 v102, s8, v223
	v_add_u32_e32 v106, s8, v224
	ds_read_b128 v[96:99], v102
	ds_read_b64 v[100:101], v106
	ds_read_b128 v[102:105], v102 offset:4096
	ds_read_b64 v[106:107], v106 offset:4096
	v_mov_b32_e32 v166, 1.0
	v_add_u32_e32 v108, s8, v221
	v_add_u32_e32 v109, s8, v222
	ds_read_b128 v[188:191], v108
	ds_read_b64 v[192:193], v109
	ds_read_b128 v[194:197], v108 offset:4096
	ds_read_b64 v[198:199], v109 offset:4096
	s_lshl_b32 s8, s15, 13
	s_add_i32 s8, s8, 0
	v_add_u32_e32 v225, s8, v163
	v_add_u32_e32 v226, s8, v220
	s_waitcnt lgkmcnt(0)
	v_mfma_scale_f32_32x32x64_f8f6f4 v[112:127], v[96:101], v[182:187], v[80:95], v217, v216 op_sel_hi:[0,0,0] cbsz:2 blgp:2
	v_mfma_scale_f32_32x32x64_f8f6f4 v[96:111], v[102:107], v[182:187], v[80:95], v217, v216 op_sel_hi:[0,0,0] cbsz:2 blgp:2
	v_mfma_scale_f32_32x32x64_f8f6f4 v[112:127], v[188:193], v[176:181], v[112:127], v217, v216 op_sel_hi:[0,0,0] cbsz:2 blgp:2
	v_mfma_scale_f32_32x32x64_f8f6f4 v[96:111], v[194:199], v[176:181], v[96:111], v217, v216 op_sel_hi:[0,0,0] cbsz:2 blgp:2
	v_exp_f32_e32 v128, v128
	v_exp_f32_e32 v129, v129
	v_exp_f32_e32 v130, v130
	v_exp_f32_e32 v131, v131
	ds_read_b128 v[206:209], v225 offset:24576
	ds_read_b64 v[210:211], v226 offset:24576
	ds_read_b128 v[200:203], v225 offset:26624
	ds_read_b64 v[204:205], v226 offset:26624
	ds_read_b128 v[194:197], v225 offset:28672
	ds_read_b64 v[198:199], v226 offset:28672
	ds_read_b128 v[188:191], v225 offset:30720
	ds_read_b64 v[192:193], v226 offset:30720
	v_exp_f32_e32 v132, v132
	v_exp_f32_e32 v133, v133
	v_exp_f32_e32 v134, v134
	v_exp_f32_e32 v135, v135
	v_exp_f32_e32 v136, v136
	v_exp_f32_e32 v137, v137
	v_exp_f32_e32 v138, v138
	v_exp_f32_e32 v139, v139
	v_exp_f32_e32 v140, v140
	v_exp_f32_e32 v141, v141
	v_exp_f32_e32 v142, v142
	v_exp_f32_e32 v143, v143
	s_nop 0
	v_cvt_scalef32_2xpk16_bf6_f32 v[128:133], v[144:159], v[128:143], 1.0
	s_nop 1
	v_mfma_scale_f32_32x32x64_f8f6f4 v[64:79], v[128:133], v[168:173], v[64:79], v218, v218 op_sel_hi:[0,0,0] cbsz:3 blgp:2
	s_waitcnt lgkmcnt(0)
	v_mfma_scale_f32_32x32x64_f8f6f4 v[0:15], v[128:133], v[206:211], v[0:15], v218, v217 op_sel_hi:[0,0,0] cbsz:3 blgp:2
	v_mfma_scale_f32_32x32x64_f8f6f4 v[48:63], v[128:133], v[200:205], v[48:63], v218, v217 op_sel_hi:[0,0,0] cbsz:3 blgp:2
	v_mfma_scale_f32_32x32x64_f8f6f4 v[32:47], v[128:133], v[194:199], v[32:47], v218, v217 op_sel_hi:[0,0,0] cbsz:3 blgp:2
	v_mfma_scale_f32_32x32x64_f8f6f4 v[16:31], v[128:133], v[188:193], v[16:31], v218, v217 op_sel_hi:[0,0,0] cbsz:3 blgp:2
	v_max_f32_e32 v225, v113, v113
	v_max_f32_e32 v226, v112, v112
	v_max_f32_e32 v225, v226, v225
	v_max3_f32 v225, v225, v114, v115
	v_max3_f32 v225, v225, v116, v117
	v_max3_f32 v225, v225, v118, v119
	v_max3_f32 v225, v225, v120, v121
	v_max3_f32 v225, v225, v122, v123
	v_max3_f32 v225, v225, v124, v125
	v_max3_f32 v225, v225, v126, v127
	v_max3_f32 v225, v225, v96, v97
	v_max3_f32 v225, v225, v98, v99
	v_max3_f32 v225, v225, v100, v101
	v_max3_f32 v225, v225, v102, v103
	v_max3_f32 v225, v225, v104, v105
	v_max3_f32 v225, v225, v106, v107
	v_max3_f32 v225, v225, v108, v109
	v_max3_f32 v225, v225, v110, v111
	v_mov_b32_e32 v226, v225
	s_nop 1
	v_permlane32_swap_b32_e32 v225, v226
	v_max_f32_e32 v226, v226, v226
	v_max_f32_e32 v225, v225, v225
	v_max_f32_e32 v225, v225, v226
	v_cmp_ge_f32_e32 vcc, s2, v225
	s_cmp_eq_u64 vcc, exec
	s_cbranch_scc0 .LBB0_444
.LBB0_420:
	v_cmp_gt_f32_e32 vcc, 1.0, v166
	s_cbranch_vccz .LBB0_424
	v_mbcnt_lo_u32_b32 v128, -1, 0
	v_mbcnt_hi_u32_b32 v128, -1, v128
	s_nop 0
	v_cmp_gt_u32_e32 vcc, 32, v128
	s_and_saveexec_b64 s[12:13], vcc
	v_lshl_add_u32 v129, v128, 2, s86
	ds_write_b32 v129, v166 offset:49152
	s_or_b64 exec, exec, s[12:13]
	v_ashrrev_i32_e32 v128, 3, v128
	v_lshlrev_b32_e32 v128, 2, v128
	v_and_b32_e32 v128, -16, v128
	s_waitcnt lgkmcnt(0)
	v_add_u32_e32 v140, s86, v128
	ds_read_b128 v[128:131], v140 offset:49248
	ds_read_b128 v[132:135], v140 offset:49216
	ds_read_b128 v[136:139], v140 offset:49184
	ds_read_b128 v[140:143], v140 offset:49152
	s_waitcnt lgkmcnt(0)
	v_pk_mul_f32 v[12:13], v[12:13], v[128:129]
	v_pk_mul_f32 v[8:9], v[8:9], v[132:133]
	v_pk_mul_f32 v[4:5], v[4:5], v[136:137]
	v_pk_mul_f32 v[14:15], v[14:15], v[130:131]
	v_pk_mul_f32 v[10:11], v[10:11], v[134:135]
	v_pk_mul_f32 v[6:7], v[6:7], v[138:139]
	v_pk_mul_f32 v[2:3], v[2:3], v[142:143]
	v_pk_mul_f32 v[0:1], v[0:1], v[140:141]
	v_pk_mul_f32 v[60:61], v[60:61], v[128:129]
	v_pk_mul_f32 v[56:57], v[56:57], v[132:133]
	v_pk_mul_f32 v[52:53], v[52:53], v[136:137]
	v_pk_mul_f32 v[62:63], v[62:63], v[130:131]
	v_pk_mul_f32 v[58:59], v[58:59], v[134:135]
	v_pk_mul_f32 v[54:55], v[54:55], v[138:139]
	v_pk_mul_f32 v[50:51], v[50:51], v[142:143]
	v_pk_mul_f32 v[48:49], v[48:49], v[140:141]
	v_pk_mul_f32 v[44:45], v[44:45], v[128:129]
	v_pk_mul_f32 v[40:41], v[40:41], v[132:133]
	v_pk_mul_f32 v[36:37], v[36:37], v[136:137]
	v_pk_mul_f32 v[46:47], v[46:47], v[130:131]
	v_pk_mul_f32 v[42:43], v[42:43], v[134:135]
	v_pk_mul_f32 v[38:39], v[38:39], v[138:139]
	v_pk_mul_f32 v[34:35], v[34:35], v[142:143]
	v_pk_mul_f32 v[32:33], v[32:33], v[140:141]
	v_pk_mul_f32 v[28:29], v[28:29], v[128:129]
	v_pk_mul_f32 v[24:25], v[24:25], v[132:133]
	v_pk_mul_f32 v[20:21], v[20:21], v[136:137]
	v_pk_mul_f32 v[30:31], v[30:31], v[130:131]
	v_pk_mul_f32 v[26:27], v[26:27], v[134:135]
	v_pk_mul_f32 v[22:23], v[22:23], v[138:139]
	v_pk_mul_f32 v[18:19], v[18:19], v[142:143]
	v_pk_mul_f32 v[16:17], v[16:17], v[140:141]
	v_pk_mul_f32 v[76:77], v[76:77], v[128:129]
	v_pk_mul_f32 v[72:73], v[72:73], v[132:133]
	v_pk_mul_f32 v[68:69], v[68:69], v[136:137]
	v_pk_mul_f32 v[78:79], v[78:79], v[130:131]
	v_pk_mul_f32 v[74:75], v[74:75], v[134:135]
	v_pk_mul_f32 v[70:71], v[70:71], v[138:139]
	v_pk_mul_f32 v[66:67], v[66:67], v[142:143]
	v_pk_mul_f32 v[64:65], v[64:65], v[140:141]
.LBB0_424:
	v_exp_f32_e32 v112, v112
	v_exp_f32_e32 v113, v113
	v_exp_f32_e32 v114, v114
	v_exp_f32_e32 v115, v115
	v_exp_f32_e32 v116, v116
	v_exp_f32_e32 v117, v117
	v_exp_f32_e32 v118, v118
	v_exp_f32_e32 v119, v119
	v_exp_f32_e32 v120, v120
	v_exp_f32_e32 v121, v121
	v_exp_f32_e32 v122, v122
	v_exp_f32_e32 v123, v123
	v_exp_f32_e32 v124, v124
	v_exp_f32_e32 v125, v125
	v_exp_f32_e32 v126, v126
	v_exp_f32_e32 v127, v127
	s_mov_b64 s[12:13], -1
	s_and_b64 vcc, exec, s[60:61]
	s_cbranch_vccz .LBB0_426
	s_waitcnt vmcnt(0) lgkmcnt(0)
	s_mov_b64 s[12:13], 0

.LBB0_437:
	s_add_i32 s8, s57, 1
	s_cmp_lg_u32 s57, 2
	s_cselect_b32 s8, s8, 0
	s_add_i32 s12, s15, 1
	s_cmp_lg_u32 s15, 2
	s_cselect_b32 s15, s12, 0
	s_lshl_b32 s12, s8, 13
	s_add_i32 s12, s12, 0
	v_add_u32_e32 v134, s12, v223
	v_add_u32_e32 v138, s12, v224
	ds_read_b128 v[128:131], v134
	ds_read_b64 v[132:133], v138
	ds_read_b128 v[134:137], v134 offset:4096
	ds_read_b64 v[138:139], v138 offset:4096
	v_mov_b32_e32 v166, 1.0
	v_add_u32_e32 v140, s12, v221
	v_add_u32_e32 v141, s12, v222
	ds_read_b128 v[188:191], v140
	ds_read_b64 v[192:193], v141
	ds_read_b128 v[194:197], v140 offset:4096
	ds_read_b64 v[198:199], v141 offset:4096
	s_lshl_b32 s12, s15, 13
	s_add_i32 s12, s12, 0
	v_add_u32_e32 v212, s12, v163
	v_add_u32_e32 v213, s12, v220
	s_waitcnt lgkmcnt(0)
	v_mfma_scale_f32_32x32x64_f8f6f4 v[144:159], v[128:133], v[182:187], v[80:95], v217, v216 op_sel_hi:[0,0,0] cbsz:2 blgp:2
	v_mfma_scale_f32_32x32x64_f8f6f4 v[128:143], v[134:139], v[182:187], v[80:95], v217, v216 op_sel_hi:[0,0,0] cbsz:2 blgp:2
	v_mfma_scale_f32_32x32x64_f8f6f4 v[144:159], v[188:193], v[176:181], v[144:159], v217, v216 op_sel_hi:[0,0,0] cbsz:2 blgp:2
	v_mfma_scale_f32_32x32x64_f8f6f4 v[128:143], v[194:199], v[176:181], v[128:143], v217, v216 op_sel_hi:[0,0,0] cbsz:2 blgp:2
	v_exp_f32_e32 v96, v96
	v_exp_f32_e32 v97, v97
	v_exp_f32_e32 v98, v98
	v_exp_f32_e32 v99, v99
	ds_read_b128 v[206:209], v212 offset:24576
	ds_read_b64 v[210:211], v213 offset:24576
	ds_read_b128 v[200:203], v212 offset:26624
	ds_read_b64 v[204:205], v213 offset:26624
	ds_read_b128 v[194:197], v212 offset:28672
	ds_read_b64 v[198:199], v213 offset:28672
	ds_read_b128 v[188:191], v212 offset:30720
	ds_read_b64 v[192:193], v213 offset:30720
	v_exp_f32_e32 v100, v100
	v_exp_f32_e32 v101, v101
	v_exp_f32_e32 v102, v102
	v_exp_f32_e32 v103, v103
	v_exp_f32_e32 v104, v104
	v_exp_f32_e32 v105, v105
	v_exp_f32_e32 v106, v106
	v_exp_f32_e32 v107, v107
	v_exp_f32_e32 v108, v108
	v_exp_f32_e32 v109, v109
	v_exp_f32_e32 v110, v110
	v_exp_f32_e32 v111, v111
	s_nop 0
	v_cvt_scalef32_2xpk16_bf6_f32 v[96:101], v[112:127], v[96:111], 1.0
	s_nop 1
	v_mfma_scale_f32_32x32x64_f8f6f4 v[64:79], v[96:101], v[168:173], v[64:79], v218, v218 op_sel_hi:[0,0,0] cbsz:3 blgp:2
	s_waitcnt lgkmcnt(0)
	v_mfma_scale_f32_32x32x64_f8f6f4 v[0:15], v[96:101], v[206:211], v[0:15], v218, v217 op_sel_hi:[0,0,0] cbsz:3 blgp:2
	v_mfma_scale_f32_32x32x64_f8f6f4 v[48:63], v[96:101], v[200:205], v[48:63], v218, v217 op_sel_hi:[0,0,0] cbsz:3 blgp:2
	v_mfma_scale_f32_32x32x64_f8f6f4 v[32:47], v[96:101], v[194:199], v[32:47], v218, v217 op_sel_hi:[0,0,0] cbsz:3 blgp:2
	v_mfma_scale_f32_32x32x64_f8f6f4 v[16:31], v[96:101], v[188:193], v[16:31], v218, v217 op_sel_hi:[0,0,0] cbsz:3 blgp:2
	v_max_f32_e32 v212, v145, v145
	v_max_f32_e32 v213, v144, v144
	v_max_f32_e32 v212, v213, v212
	v_max3_f32 v212, v212, v146, v147
	v_max3_f32 v212, v212, v148, v149
	v_max3_f32 v212, v212, v150, v151
	v_max3_f32 v212, v212, v152, v153
	v_max3_f32 v212, v212, v154, v155
	v_max3_f32 v212, v212, v156, v157
	v_max3_f32 v212, v212, v158, v159
	v_max3_f32 v212, v212, v128, v129
	v_max3_f32 v212, v212, v130, v131
	v_max3_f32 v212, v212, v132, v133
	v_max3_f32 v212, v212, v134, v135
	v_max3_f32 v212, v212, v136, v137
	v_max3_f32 v212, v212, v138, v139
	v_max3_f32 v212, v212, v140, v141
	v_max3_f32 v212, v212, v142, v143
	v_mov_b32_e32 v213, v212
	s_nop 1
	v_permlane32_swap_b32_e32 v212, v213
	v_max_f32_e32 v213, v213, v213
	v_max_f32_e32 v212, v212, v212
	v_max_f32_e32 v212, v212, v213
	v_cmp_ge_f32_e32 vcc, s2, v212
	s_cmp_eq_u64 vcc, exec
	s_cbranch_scc0 .LBB0_445
.LBB0_438:
	v_cmp_gt_f32_e32 vcc, 1.0, v166
	s_cbranch_vccz .LBB0_442
	v_mbcnt_lo_u32_b32 v96, -1, 0
	v_mbcnt_hi_u32_b32 v96, -1, v96
	s_nop 0
	v_cmp_gt_u32_e32 vcc, 32, v96
	s_and_saveexec_b64 s[12:13], vcc
	v_lshl_add_u32 v97, v96, 2, s86
	ds_write_b32 v97, v166 offset:49152
	s_or_b64 exec, exec, s[12:13]
	v_ashrrev_i32_e32 v96, 3, v96
	v_lshlrev_b32_e32 v96, 2, v96
	v_and_b32_e32 v96, -16, v96
	s_waitcnt lgkmcnt(0)
	v_add_u32_e32 v108, s86, v96
	ds_read_b128 v[96:99], v108 offset:49248
	ds_read_b128 v[100:103], v108 offset:49216
	ds_read_b128 v[104:107], v108 offset:49184
	ds_read_b128 v[108:111], v108 offset:49152
	s_waitcnt lgkmcnt(0)
	v_pk_mul_f32 v[12:13], v[12:13], v[96:97]
	v_pk_mul_f32 v[8:9], v[8:9], v[100:101]
	v_pk_mul_f32 v[4:5], v[4:5], v[104:105]
	v_pk_mul_f32 v[14:15], v[14:15], v[98:99]
	v_pk_mul_f32 v[10:11], v[10:11], v[102:103]
	v_pk_mul_f32 v[6:7], v[6:7], v[106:107]
	v_pk_mul_f32 v[2:3], v[2:3], v[110:111]
	v_pk_mul_f32 v[0:1], v[0:1], v[108:109]
	v_pk_mul_f32 v[60:61], v[60:61], v[96:97]
	v_pk_mul_f32 v[56:57], v[56:57], v[100:101]
	v_pk_mul_f32 v[52:53], v[52:53], v[104:105]
	v_pk_mul_f32 v[62:63], v[62:63], v[98:99]
	v_pk_mul_f32 v[58:59], v[58:59], v[102:103]
	v_pk_mul_f32 v[54:55], v[54:55], v[106:107]
	v_pk_mul_f32 v[50:51], v[50:51], v[110:111]
	v_pk_mul_f32 v[48:49], v[48:49], v[108:109]
	v_pk_mul_f32 v[44:45], v[44:45], v[96:97]
	v_pk_mul_f32 v[40:41], v[40:41], v[100:101]
	v_pk_mul_f32 v[36:37], v[36:37], v[104:105]
	v_pk_mul_f32 v[46:47], v[46:47], v[98:99]
	v_pk_mul_f32 v[42:43], v[42:43], v[102:103]
	v_pk_mul_f32 v[38:39], v[38:39], v[106:107]
	v_pk_mul_f32 v[34:35], v[34:35], v[110:111]
	v_pk_mul_f32 v[32:33], v[32:33], v[108:109]
	v_pk_mul_f32 v[28:29], v[28:29], v[96:97]
	v_pk_mul_f32 v[24:25], v[24:25], v[100:101]
	v_pk_mul_f32 v[20:21], v[20:21], v[104:105]
	v_pk_mul_f32 v[30:31], v[30:31], v[98:99]
	v_pk_mul_f32 v[26:27], v[26:27], v[102:103]
	v_pk_mul_f32 v[22:23], v[22:23], v[106:107]
	v_pk_mul_f32 v[18:19], v[18:19], v[110:111]
	v_pk_mul_f32 v[16:17], v[16:17], v[108:109]
	v_pk_mul_f32 v[76:77], v[76:77], v[96:97]
	v_pk_mul_f32 v[72:73], v[72:73], v[100:101]
	v_pk_mul_f32 v[68:69], v[68:69], v[104:105]
	v_pk_mul_f32 v[78:79], v[78:79], v[98:99]
	v_pk_mul_f32 v[74:75], v[74:75], v[102:103]
	v_pk_mul_f32 v[70:71], v[70:71], v[106:107]
	v_pk_mul_f32 v[66:67], v[66:67], v[110:111]
	v_pk_mul_f32 v[64:65], v[64:65], v[108:109]
